# first grid barrier: the 16 per-XCD counters requested together; MoeOrder::next in M1's table set-up (9 copies) vectorised like the loop-top one; on top of m12
# speedup vs baseline: 1.0252x; 1.0039x over previous
; DI unsigned xb_ld(unsigned* p)              { return __hip_atomic_load(p, __ATOMIC_RELAXED, __HIP_MEMORY_SCOPE_AGENT); }
; DI void xcd_barrier_complete(unsigned* bar, unsigned x, unsigned& nloc, unsigned& nx) {
;     ...
;     for (;;) {
;         sum = 0u; cnt = 0u; mine = 0u;
; #pragma unroll
;         for (unsigned j = 0; j < 16; ++j) { const unsigned c = xb_ld(&bar[XB_XCNT(j)]); sum += c; cnt += (c > 0u) ? 1u : 0u; mine = (j == x) ? c : mine; }
;         if (sum == G) break;
;         __builtin_amdgcn_s_sleep(1);
;         if ((++sp & 255u) == 0u) { if (xb_ld(&bar[XB_TMO])) break; if (sp > XB_SPIN_CAP) { atomicAdd(&bar[XB_TMO], 1u); break; } }
;     }
.LBB0_220:
	v_mov_b64_e32 v[18:19], s[96:97]
	flat_load_dword v1, v[18:19] sc1
	flat_load_dword v2, v[18:19] offset:256 sc1
	flat_load_dword v3, v[18:19] offset:512 sc1
	flat_load_dword v5, v[18:19] offset:768 sc1
	flat_load_dword v6, v[18:19] offset:1024 sc1
	flat_load_dword v7, v[18:19] offset:1280 sc1
	flat_load_dword v8, v[18:19] offset:1536 sc1
	flat_load_dword v9, v[18:19] offset:1792 sc1
	flat_load_dword v10, v[18:19] offset:2048 sc1
	flat_load_dword v11, v[18:19] offset:2304 sc1
	flat_load_dword v12, v[18:19] offset:2560 sc1
	flat_load_dword v13, v[18:19] offset:2816 sc1
	flat_load_dword v14, v[18:19] offset:3072 sc1
	flat_load_dword v15, v[18:19] offset:3328 sc1
	flat_load_dword v16, v[18:19] offset:3584 sc1
	flat_load_dword v17, v[18:19] offset:3840 sc1
	s_or_b64 s[44:45], s[44:45], exec
	s_or_b64 s[42:43], s[42:43], exec
	s_waitcnt vmcnt(0) lgkmcnt(0)
	v_add_u32_e32 v18, v2, v1
	v_add3_u32 v18, v18, v3, v5
	v_add3_u32 v18, v18, v6, v7
	v_add3_u32 v18, v18, v8, v9
	v_add3_u32 v18, v18, v10, v11
	v_add3_u32 v18, v18, v12, v13
	v_add3_u32 v18, v18, v14, v15
	v_add3_u32 v18, v18, v16, v17
	v_cmp_ne_u32_e32 vcc, s4, v18
	s_and_saveexec_b64 s[46:47], vcc
	s_cbranch_execz .LBB0_219
	s_and_b32 s5, s1, 0xff
	s_mov_b64 s[48:49], -1
	s_cmp_eq_u32 s5, 0
	s_mov_b64 s[52:53], -1
	s_mov_b64 s[50:51], -1
	s_sleep 1
	s_cbranch_scc1 .LBB0_223
	s_and_saveexec_b64 s[54:55], s[52:53]
	s_cbranch_execz .LBB0_218
	s_branch .LBB0_226

; DI int rfl(int v) { return __builtin_amdgcn_readfirstlane(v); }
; DI int ltid() { int t = threadIdx.x; asm volatile("" : "+v"(t)); return t; }
;     DI bool next(int i, Unit& u) const {
;         const int L = i * G + c; if (L >= ntot) return false;
;         const int rt = L / NC; u.pn = L - rt * NC; u.pm = rt;
;         int e = 0;
; #pragma unroll
;         for (int j = 1; j < 16; ++j) e += (rt >= rfl(pre[j])) ? 1 : 0;
;         e = rfl(e); u.e = e; const int rem = rfl(cnt[e]) - 256 * (rt - rfl(pre[e])); u.nv = rem < 256 ? rem : 256; u.ui = i; return true;
; __global__ void __launch_bounds__(NTHREADS, 2) mk_fwd(Ctx c_arg) {
;     ...
;             { const int lt_tid = ltid(); const int r = lt_tid & 255, half = rfl(lt_tid >> 8);
;               int tv[MAXU / 2];
; #pragma unroll
;               for (int k = 0; k < MAXU / 2; ++k) { Unit u; const int i = 2 * k + half; tv[k] = 0;
;                   if (S.next(i, u)) { const int lt = u.pm - PRE[u.e]; const int pos = 256 * lt + (r < u.nv ? r : 0); tv[k] = list[(size_t)u.e * T + pos]; } }
.LBB0_1297:
	s_add_i32 s1, s38, 0x27f04
	v_writelane_b32 v254, s1, 38
	s_add_i32 s1, s38, 0x27f08
	v_writelane_b32 v254, s1, 34
	s_add_i32 s1, s38, 0x27f0c
	v_writelane_b32 v254, s1, 36
	s_add_i32 s1, s38, 0x27f10
	v_writelane_b32 v254, s1, 30
	s_add_i32 s1, s38, 0x27f14
	v_writelane_b32 v254, s1, 28
	s_add_i32 s1, s38, 0x27f18
	v_writelane_b32 v254, s1, 62
	s_add_i32 s1, s38, 0x27f1c
	v_writelane_b32 v255, s1, 36
	s_add_i32 s1, s38, 0x27f20
	v_mov_b32_e32 v1, v0
	v_writelane_b32 v255, s1, 16
	s_add_i32 s1, s38, 0x27f24
	s_lshl_b32 s79, s0, 3
	v_writelane_b32 v255, s1, 20
	v_readfirstlane_b32 s0, v1
	s_add_i32 s1, s38, 0x27f28
	s_ashr_i32 s0, s0, 8
	v_writelane_b32 v255, s1, 26
	s_add_i32 s1, s38, 0x27f2c
	v_writelane_b32 v254, s1, 57
	s_add_i32 s1, s38, 0x27f30
	s_mul_i32 s6, s0, s39
	v_writelane_b32 v255, s1, 18
	s_add_i32 s1, s38, 0x27f34
	s_add_i32 s93, s38, 0x27f38
	s_add_i32 s94, s38, 0x27f3c
	s_add_i32 s6, s6, s78
	s_cmp_lt_i32 s6, s79
	v_writelane_b32 v255, s1, 0
	s_cselect_b64 s[16:17], -1, 0
	s_cmp_ge_i32 s6, s79
	s_cbranch_scc1 .LBB0_1299
	s_ashr_i32 s1, s6, 31
	s_lshr_b32 s1, s1, 29
	s_add_i32 s1, s6, s1
	s_ashr_i32 s7, s1, 3
	v_lshl_add_u32 v2, v202, 2, s76
	ds_read_b32 v2, v2
	s_waitcnt lgkmcnt(0)
	v_cmp_ge_i32_e32 vcc, s7, v2
	s_and_b32 s8, vcc_lo, 0xfffe
	s_bcnt1_i32_b32 s8, s8
	s_mov_b32 s4, s8
	v_writelane_b32 v254, s4, 20
	s_lshl_b32 s1, s8, 2
	v_writelane_b32 v255, s7, 40
	v_writelane_b32 v254, s5, 21
	s_add_i32 s4, s13, s1
	s_add_i32 s1, s76, s1
	v_mov_b32_e32 v2, s4
	v_mov_b32_e32 v3, s1
	ds_read_b32 v2, v2
	ds_read_b32 v3, v3
	s_waitcnt lgkmcnt(1)
	v_readfirstlane_b32 s1, v2
	s_waitcnt lgkmcnt(0)
	v_readfirstlane_b32 s4, v3
	s_sub_i32 s4, s4, s7
	s_lshl_b32 s4, s4, 8
	s_add_i32 s4, s4, s1
	s_min_i32 s1, s4, 0x100
	v_writelane_b32 v255, s1, 41

; DI int rfl(int v) { return __builtin_amdgcn_readfirstlane(v); }
; DI int ltid() { int t = threadIdx.x; asm volatile("" : "+v"(t)); return t; }
;     DI bool next(int i, Unit& u) const {
;         const int L = i * G + c; if (L >= ntot) return false;
;         const int rt = L / NC; u.pn = L - rt * NC; u.pm = rt;
;         int e = 0;
; #pragma unroll
;         for (int j = 1; j < 16; ++j) e += (rt >= rfl(pre[j])) ? 1 : 0;
;         e = rfl(e); u.e = e; const int rem = rfl(cnt[e]) - 256 * (rt - rfl(pre[e])); u.nv = rem < 256 ? rem : 256; u.ui = i; return true;
; __global__ void __launch_bounds__(NTHREADS, 2) mk_fwd(Ctx c_arg) {
;     ...
;             { const int lt_tid = ltid(); const int r = lt_tid & 255, half = rfl(lt_tid >> 8);
;               int tv[MAXU / 2];
; #pragma unroll
;               for (int k = 0; k < MAXU / 2; ++k) { Unit u; const int i = 2 * k + half; tv[k] = 0;
;                   if (S.next(i, u)) { const int lt = u.pm - PRE[u.e]; const int pos = 256 * lt + (r < u.nv ? r : 0); tv[k] = list[(size_t)u.e * T + pos]; } }
.LBB0_1301:
	s_lshl_b32 s5, s39, 1
	s_add_i32 s6, s6, s5
	s_cmp_lt_i32 s6, s79
	s_cselect_b64 s[42:43], -1, 0
	s_cmp_ge_i32 s6, s79
	s_cbranch_scc1 .LBB0_1303
	s_ashr_i32 s7, s6, 31
	s_lshr_b32 s7, s7, 29
	s_add_i32 s7, s6, s7
	s_ashr_i32 s10, s7, 3
	v_lshl_add_u32 v1, v202, 2, s76
	ds_read_b32 v1, v1
	s_waitcnt lgkmcnt(0)
	v_cmp_ge_i32_e32 vcc, s10, v1
	s_and_b32 s30, vcc_lo, 0xfffe
	s_bcnt1_i32_b32 s30, s30
	s_mov_b32 s8, s30
	v_writelane_b32 v254, s8, 20
	s_lshl_b32 s7, s30, 2
	v_writelane_b32 v255, s10, 40
	v_writelane_b32 v254, s9, 21
	s_add_i32 s8, s13, s7
	s_add_i32 s7, s76, s7
	v_mov_b32_e32 v1, s8
	v_mov_b32_e32 v3, s7
	ds_read_b32 v1, v1
	ds_read_b32 v3, v3
	s_waitcnt lgkmcnt(1)
	v_readfirstlane_b32 s7, v1
	s_waitcnt lgkmcnt(0)
	v_readfirstlane_b32 s8, v3
	s_sub_i32 s8, s8, s10
	s_lshl_b32 s8, s8, 8
	s_add_i32 s8, s8, s7
	s_min_i32 s7, s8, 0x100
	v_writelane_b32 v255, s7, 41

; DI int rfl(int v) { return __builtin_amdgcn_readfirstlane(v); }
; DI int ltid() { int t = threadIdx.x; asm volatile("" : "+v"(t)); return t; }
;     DI bool next(int i, Unit& u) const {
;         const int L = i * G + c; if (L >= ntot) return false;
;         const int rt = L / NC; u.pn = L - rt * NC; u.pm = rt;
;         int e = 0;
; #pragma unroll
;         for (int j = 1; j < 16; ++j) e += (rt >= rfl(pre[j])) ? 1 : 0;
;         e = rfl(e); u.e = e; const int rem = rfl(cnt[e]) - 256 * (rt - rfl(pre[e])); u.nv = rem < 256 ? rem : 256; u.ui = i; return true;
; __global__ void __launch_bounds__(NTHREADS, 2) mk_fwd(Ctx c_arg) {
;     ...
;             { const int lt_tid = ltid(); const int r = lt_tid & 255, half = rfl(lt_tid >> 8);
;               int tv[MAXU / 2];
; #pragma unroll
;               for (int k = 0; k < MAXU / 2; ++k) { Unit u; const int i = 2 * k + half; tv[k] = 0;
;                   if (S.next(i, u)) { const int lt = u.pm - PRE[u.e]; const int pos = 256 * lt + (r < u.nv ? r : 0); tv[k] = list[(size_t)u.e * T + pos]; } }
.LBB0_1306:
	s_add_i32 s6, s6, s5
	s_cmp_lt_i32 s6, s79
	s_cselect_b64 s[44:45], -1, 0
	s_cmp_ge_i32 s6, s79
	s_cbranch_scc1 .LBB0_1308
	s_ashr_i32 s7, s6, 31
	s_lshr_b32 s7, s7, 29
	s_add_i32 s7, s6, s7
	s_ashr_i32 s10, s7, 3
	v_lshl_add_u32 v3, v202, 2, s76
	ds_read_b32 v3, v3
	s_waitcnt lgkmcnt(0)
	v_cmp_ge_i32_e32 vcc, s10, v3
	s_and_b32 s30, vcc_lo, 0xfffe
	s_bcnt1_i32_b32 s30, s30
	s_mov_b32 s8, s30
	v_writelane_b32 v254, s8, 20
	s_lshl_b32 s7, s30, 2
	v_writelane_b32 v255, s10, 40
	v_writelane_b32 v254, s9, 21
	s_add_i32 s8, s13, s7
	s_add_i32 s7, s76, s7
	v_mov_b32_e32 v3, s8
	v_mov_b32_e32 v5, s7
	ds_read_b32 v3, v3
	ds_read_b32 v5, v5
	s_waitcnt lgkmcnt(1)
	v_readfirstlane_b32 s7, v3
	s_waitcnt lgkmcnt(0)
	v_readfirstlane_b32 s8, v5
	s_sub_i32 s8, s8, s10
	s_lshl_b32 s8, s8, 8
	s_add_i32 s8, s8, s7
	s_min_i32 s7, s8, 0x100
	v_writelane_b32 v255, s7, 41

; DI int rfl(int v) { return __builtin_amdgcn_readfirstlane(v); }
; DI int ltid() { int t = threadIdx.x; asm volatile("" : "+v"(t)); return t; }
;     DI bool next(int i, Unit& u) const {
;         const int L = i * G + c; if (L >= ntot) return false;
;         const int rt = L / NC; u.pn = L - rt * NC; u.pm = rt;
;         int e = 0;
; #pragma unroll
;         for (int j = 1; j < 16; ++j) e += (rt >= rfl(pre[j])) ? 1 : 0;
;         e = rfl(e); u.e = e; const int rem = rfl(cnt[e]) - 256 * (rt - rfl(pre[e])); u.nv = rem < 256 ? rem : 256; u.ui = i; return true;
; __global__ void __launch_bounds__(NTHREADS, 2) mk_fwd(Ctx c_arg) {
;     ...
;             { const int lt_tid = ltid(); const int r = lt_tid & 255, half = rfl(lt_tid >> 8);
;               int tv[MAXU / 2];
; #pragma unroll
;               for (int k = 0; k < MAXU / 2; ++k) { Unit u; const int i = 2 * k + half; tv[k] = 0;
;                   if (S.next(i, u)) { const int lt = u.pm - PRE[u.e]; const int pos = 256 * lt + (r < u.nv ? r : 0); tv[k] = list[(size_t)u.e * T + pos]; } }
.LBB0_1311:
	s_add_i32 s6, s6, s5
	s_cmp_lt_i32 s6, s79
	s_cselect_b64 s[46:47], -1, 0
	s_cmp_ge_i32 s6, s79
	s_cbranch_scc1 .LBB0_1313
	s_ashr_i32 s7, s6, 31
	s_lshr_b32 s7, s7, 29
	s_add_i32 s7, s6, s7
	s_ashr_i32 s10, s7, 3
	v_lshl_add_u32 v3, v202, 2, s76
	ds_read_b32 v3, v3
	s_waitcnt lgkmcnt(0)
	v_cmp_ge_i32_e32 vcc, s10, v3
	s_and_b32 s30, vcc_lo, 0xfffe
	s_bcnt1_i32_b32 s30, s30
	s_mov_b32 s8, s30
	v_writelane_b32 v254, s8, 20
	s_lshl_b32 s7, s30, 2
	v_writelane_b32 v255, s10, 40
	v_writelane_b32 v254, s9, 21
	s_add_i32 s8, s13, s7
	s_add_i32 s7, s76, s7
	v_mov_b32_e32 v3, s8
	v_mov_b32_e32 v5, s7
	ds_read_b32 v3, v3
	ds_read_b32 v5, v5
	s_waitcnt lgkmcnt(1)
	v_readfirstlane_b32 s7, v3
	s_waitcnt lgkmcnt(0)
	v_readfirstlane_b32 s8, v5
	s_sub_i32 s8, s8, s10
	s_lshl_b32 s8, s8, 8
	s_add_i32 s8, s8, s7
	s_min_i32 s7, s8, 0x100
	v_writelane_b32 v255, s7, 41

; DI int rfl(int v) { return __builtin_amdgcn_readfirstlane(v); }
; DI int ltid() { int t = threadIdx.x; asm volatile("" : "+v"(t)); return t; }
;     DI bool next(int i, Unit& u) const {
;         const int L = i * G + c; if (L >= ntot) return false;
;         const int rt = L / NC; u.pn = L - rt * NC; u.pm = rt;
;         int e = 0;
; #pragma unroll
;         for (int j = 1; j < 16; ++j) e += (rt >= rfl(pre[j])) ? 1 : 0;
;         e = rfl(e); u.e = e; const int rem = rfl(cnt[e]) - 256 * (rt - rfl(pre[e])); u.nv = rem < 256 ? rem : 256; u.ui = i; return true;
; __global__ void __launch_bounds__(NTHREADS, 2) mk_fwd(Ctx c_arg) {
;     ...
;             { const int lt_tid = ltid(); const int r = lt_tid & 255, half = rfl(lt_tid >> 8);
;               int tv[MAXU / 2];
; #pragma unroll
;               for (int k = 0; k < MAXU / 2; ++k) { Unit u; const int i = 2 * k + half; tv[k] = 0;
;                   if (S.next(i, u)) { const int lt = u.pm - PRE[u.e]; const int pos = 256 * lt + (r < u.nv ? r : 0); tv[k] = list[(size_t)u.e * T + pos]; } }
.LBB0_1316:
	s_add_i32 s6, s6, s5
	s_cmp_lt_i32 s6, s79
	s_cselect_b64 s[48:49], -1, 0
	s_cmp_ge_i32 s6, s79
	s_cbranch_scc1 .LBB0_1318
	s_ashr_i32 s7, s6, 31
	s_lshr_b32 s7, s7, 29
	s_add_i32 s7, s6, s7
	s_ashr_i32 s10, s7, 3
	v_lshl_add_u32 v5, v202, 2, s76
	ds_read_b32 v5, v5
	s_waitcnt lgkmcnt(0)
	v_cmp_ge_i32_e32 vcc, s10, v5
	s_and_b32 s30, vcc_lo, 0xfffe
	s_bcnt1_i32_b32 s30, s30
	s_mov_b32 s8, s30
	v_writelane_b32 v254, s8, 20
	s_lshl_b32 s7, s30, 2
	v_writelane_b32 v255, s10, 40
	v_writelane_b32 v254, s9, 21
	s_add_i32 s8, s13, s7
	s_add_i32 s7, s76, s7
	v_mov_b32_e32 v5, s8
	v_mov_b32_e32 v7, s7
	ds_read_b32 v5, v5
	ds_read_b32 v7, v7
	s_waitcnt lgkmcnt(1)
	v_readfirstlane_b32 s7, v5
	s_waitcnt lgkmcnt(0)
	v_readfirstlane_b32 s8, v7
	s_sub_i32 s8, s8, s10
	s_lshl_b32 s8, s8, 8
	s_add_i32 s8, s8, s7
	s_min_i32 s7, s8, 0x100
	v_writelane_b32 v255, s7, 41

; DI int rfl(int v) { return __builtin_amdgcn_readfirstlane(v); }
;     DI bool next(int i, Unit& u) const {
;         const int L = i * G + c; if (L >= ntot) return false;
;         const int rt = L / NC; u.pn = L - rt * NC; u.pm = rt;
;         int e = 0;
; #pragma unroll
;         for (int j = 1; j < 16; ++j) e += (rt >= rfl(pre[j])) ? 1 : 0;
;         e = rfl(e); u.e = e; const int rem = rfl(cnt[e]) - 256 * (rt - rfl(pre[e])); u.nv = rem < 256 ? rem : 256; u.ui = i; return true;
; __global__ void __launch_bounds__(NTHREADS, 2) mk_fwd(Ctx c_arg) {
;     ...
;               for (int k = 0; k < MAXU / 2; ++k) { Unit u; const int i = 2 * k + half; tv[k] = 0;
;                   if (S.next(i, u)) { const int lt = u.pm - PRE[u.e]; const int pos = 256 * lt + (r < u.nv ? r : 0); tv[k] = list[(size_t)u.e * T + pos]; } }
.LBB0_1321:
	s_add_i32 s6, s6, s5
	s_cmp_lt_i32 s6, s79
	s_cselect_b64 s[50:51], -1, 0
	s_cmp_ge_i32 s6, s79
	s_cbranch_scc1 .LBB0_1323
	s_ashr_i32 s7, s6, 31
	s_lshr_b32 s7, s7, 29
	s_add_i32 s7, s6, s7
	s_ashr_i32 s10, s7, 3
	v_lshl_add_u32 v5, v202, 2, s76
	ds_read_b32 v5, v5
	s_waitcnt lgkmcnt(0)
	v_cmp_ge_i32_e32 vcc, s10, v5
	s_and_b32 s30, vcc_lo, 0xfffe
	s_bcnt1_i32_b32 s30, s30
	s_mov_b32 s8, s30
	v_writelane_b32 v254, s8, 20
	s_lshl_b32 s7, s30, 2
	v_writelane_b32 v255, s10, 40
	v_writelane_b32 v254, s9, 21
	s_add_i32 s8, s13, s7
	s_add_i32 s7, s76, s7
	v_mov_b32_e32 v5, s8
	v_mov_b32_e32 v7, s7
	ds_read_b32 v5, v5
	ds_read_b32 v7, v7
	s_waitcnt lgkmcnt(1)
	v_readfirstlane_b32 s7, v5
	s_waitcnt lgkmcnt(0)
	v_readfirstlane_b32 s8, v7
	s_sub_i32 s8, s8, s10
	s_lshl_b32 s8, s8, 8
	s_add_i32 s8, s8, s7
	s_min_i32 s7, s8, 0x100
	v_writelane_b32 v255, s7, 41

; DI int rfl(int v) { return __builtin_amdgcn_readfirstlane(v); }
;     DI bool next(int i, Unit& u) const {
;         const int L = i * G + c; if (L >= ntot) return false;
;         const int rt = L / NC; u.pn = L - rt * NC; u.pm = rt;
;         int e = 0;
; #pragma unroll
;         for (int j = 1; j < 16; ++j) e += (rt >= rfl(pre[j])) ? 1 : 0;
;         e = rfl(e); u.e = e; const int rem = rfl(cnt[e]) - 256 * (rt - rfl(pre[e])); u.nv = rem < 256 ? rem : 256; u.ui = i; return true;
; __global__ void __launch_bounds__(NTHREADS, 2) mk_fwd(Ctx c_arg) {
;     ...
;               for (int k = 0; k < MAXU / 2; ++k) { Unit u; const int i = 2 * k + half; tv[k] = 0;
;                   if (S.next(i, u)) { const int lt = u.pm - PRE[u.e]; const int pos = 256 * lt + (r < u.nv ? r : 0); tv[k] = list[(size_t)u.e * T + pos]; } }
.LBB0_1326:
	s_add_i32 s6, s6, s5
	s_cmp_lt_i32 s6, s79
	s_cselect_b64 s[52:53], -1, 0
	s_cmp_ge_i32 s6, s79
	s_cbranch_scc1 .LBB0_1328
	s_ashr_i32 s7, s6, 31
	s_lshr_b32 s7, s7, 29
	s_add_i32 s7, s6, s7
	s_ashr_i32 s10, s7, 3
	v_lshl_add_u32 v7, v202, 2, s76
	ds_read_b32 v7, v7
	s_waitcnt lgkmcnt(0)
	v_cmp_ge_i32_e32 vcc, s10, v7
	s_and_b32 s30, vcc_lo, 0xfffe
	s_bcnt1_i32_b32 s30, s30
	s_mov_b32 s8, s30
	v_writelane_b32 v254, s8, 20
	s_lshl_b32 s7, s30, 2
	v_writelane_b32 v255, s10, 40
	v_writelane_b32 v254, s9, 21
	s_add_i32 s8, s13, s7
	s_add_i32 s7, s76, s7
	v_mov_b32_e32 v7, s8
	v_mov_b32_e32 v10, s7
	ds_read_b32 v7, v7
	ds_read_b32 v10, v10
	s_waitcnt lgkmcnt(1)
	v_readfirstlane_b32 s7, v7
	s_waitcnt lgkmcnt(0)
	v_readfirstlane_b32 s8, v10
	s_sub_i32 s8, s8, s10
	s_lshl_b32 s8, s8, 8
	s_add_i32 s8, s8, s7
	s_min_i32 s7, s8, 0x100
	v_writelane_b32 v255, s7, 41

; DI int rfl(int v) { return __builtin_amdgcn_readfirstlane(v); }
;     DI bool next(int i, Unit& u) const {
;         const int L = i * G + c; if (L >= ntot) return false;
;         const int rt = L / NC; u.pn = L - rt * NC; u.pm = rt;
;         int e = 0;
; #pragma unroll
;         for (int j = 1; j < 16; ++j) e += (rt >= rfl(pre[j])) ? 1 : 0;
;         e = rfl(e); u.e = e; const int rem = rfl(cnt[e]) - 256 * (rt - rfl(pre[e])); u.nv = rem < 256 ? rem : 256; u.ui = i; return true;
; __global__ void __launch_bounds__(NTHREADS, 2) mk_fwd(Ctx c_arg) {
;     ...
;               for (int k = 0; k < MAXU / 2; ++k) { Unit u; const int i = 2 * k + half; tv[k] = 0;
;                   if (S.next(i, u)) { const int lt = u.pm - PRE[u.e]; const int pos = 256 * lt + (r < u.nv ? r : 0); tv[k] = list[(size_t)u.e * T + pos]; } }
.LBB0_1331:
	s_add_i32 s6, s6, s5
	s_cmp_lt_i32 s6, s79
	s_cselect_b64 s[54:55], -1, 0
	s_cmp_ge_i32 s6, s79
	s_cbranch_scc1 .LBB0_1333
	s_ashr_i32 s7, s6, 31
	s_lshr_b32 s7, s7, 29
	s_add_i32 s7, s6, s7
	s_ashr_i32 s10, s7, 3
	v_lshl_add_u32 v7, v202, 2, s76
	ds_read_b32 v7, v7
	s_waitcnt lgkmcnt(0)
	v_cmp_ge_i32_e32 vcc, s10, v7
	s_and_b32 s30, vcc_lo, 0xfffe
	s_bcnt1_i32_b32 s30, s30
	s_mov_b32 s8, s30
	v_writelane_b32 v254, s8, 20
	s_lshl_b32 s7, s30, 2
	v_writelane_b32 v255, s10, 40
	v_writelane_b32 v254, s9, 21
	s_add_i32 s8, s13, s7
	s_add_i32 s7, s76, s7
	v_mov_b32_e32 v7, s8
	v_mov_b32_e32 v11, s7
	ds_read_b32 v7, v7
	ds_read_b32 v11, v11
	s_waitcnt lgkmcnt(1)
	v_readfirstlane_b32 s7, v7
	s_waitcnt lgkmcnt(0)
	v_readfirstlane_b32 s8, v11
	s_sub_i32 s8, s8, s10
	s_lshl_b32 s8, s8, 8
	s_add_i32 s8, s8, s7
	s_min_i32 s7, s8, 0x100
	v_writelane_b32 v255, s7, 41

; DI int rfl(int v) { return __builtin_amdgcn_readfirstlane(v); }
;     DI bool next(int i, Unit& u) const {
;         const int L = i * G + c; if (L >= ntot) return false;
;         const int rt = L / NC; u.pn = L - rt * NC; u.pm = rt;
;         int e = 0;
; #pragma unroll
;         for (int j = 1; j < 16; ++j) e += (rt >= rfl(pre[j])) ? 1 : 0;
;         e = rfl(e); u.e = e; const int rem = rfl(cnt[e]) - 256 * (rt - rfl(pre[e])); u.nv = rem < 256 ? rem : 256; u.ui = i; return true;
; __global__ void __launch_bounds__(NTHREADS, 2) mk_fwd(Ctx c_arg) {
;     ...
;               for (int k = 0; k < MAXU / 2; ++k) { Unit u; const int i = 2 * k + half; tv[k] = 0;
;                   if (S.next(i, u)) { const int lt = u.pm - PRE[u.e]; const int pos = 256 * lt + (r < u.nv ? r : 0); tv[k] = list[(size_t)u.e * T + pos]; } }
.LBB0_1336:
	s_add_i32 s5, s6, s5
	s_cmp_lt_i32 s5, s79
	s_cselect_b64 s[56:57], -1, 0
	s_cmp_ge_i32 s5, s79
	s_cbranch_scc1 .LBB0_1338
	s_ashr_i32 s6, s5, 31
	s_lshr_b32 s6, s6, 29
	s_add_i32 s5, s5, s6
	s_ashr_i32 s8, s5, 3
	v_lshl_add_u32 v11, v202, 2, s76
	ds_read_b32 v11, v11
	s_waitcnt lgkmcnt(0)
	v_cmp_ge_i32_e32 vcc, s8, v11
	s_and_b32 s10, vcc_lo, 0xfffe
	s_bcnt1_i32_b32 s10, s10
	s_mov_b32 s6, s10
	v_writelane_b32 v254, s6, 20
	s_lshl_b32 s5, s10, 2
	v_writelane_b32 v255, s8, 40
	v_writelane_b32 v254, s7, 21
	s_add_i32 s6, s13, s5
	s_add_i32 s5, s76, s5
	v_mov_b32_e32 v11, s6
	v_mov_b32_e32 v12, s5
	ds_read_b32 v11, v11
	ds_read_b32 v12, v12
	s_waitcnt lgkmcnt(1)
	v_readfirstlane_b32 s5, v11
	s_waitcnt lgkmcnt(0)
	v_readfirstlane_b32 s6, v12
	s_sub_i32 s6, s6, s8
	s_lshl_b32 s6, s6, 8
	s_add_i32 s6, s6, s5
	s_min_i32 s5, s6, 0x100
	v_writelane_b32 v255, s5, 41
